# expert GEMM epilogues: non-temporal stores for the activation and expert-output rows
# baseline (speedup 1.0000x reference)
.LBB0_1485:
	s_lshl_b32 s1, s30, 7
	s_ashr_i32 s0, s30, 4
	s_and_b32 s1, s1, 0x780
	v_or_b32_e32 v170, s1, v184
	v_lshl_add_u32 v20, s28, 8, v182
	v_fmamk_f32 v0, v158, 0x3a800000, v224
	v_fmamk_f32 v23, v156, 0x3a800000, v230
	v_fmamk_f32 v18, v154, 0x3a800000, v228
	v_min_f32_e32 v0, 0x40e00000, v0
	v_min_f32_e32 v23, 0x40e00000, v23
	v_min_f32_e32 v18, 0x40e00000, v18
	v_fmamk_f32 v26, v150, 0x3a800000, v232
	v_mul_f32_e32 v28, 0x3fd9db23, v0
	v_mul_f32_e32 v150, 0x3fd9db23, v23
	v_mul_f32_e32 v29, 0x3fd9db23, v18
	v_mul_f32_e32 v28, 0xbfb8aa3b, v28
	v_mul_f32_e32 v150, 0xbfb8aa3b, v150
	v_mul_f32_e32 v29, 0xbfb8aa3b, v29
	v_exp_f32_e32 v28, v28
	v_exp_f32_e32 v150, v150
	v_fmamk_f32 v31, v147, 0x3a800000, v237
	v_exp_f32_e32 v29, v29
	v_fmamk_f32 v21, v155, 0x3a800000, v229
	v_fmamk_f32 v27, v146, 0x3a800000, v236
	v_med3_f32 v26, v26, s59, v189
	v_med3_f32 v31, v31, s59, v189
	v_min_f32_e32 v21, 0x40e00000, v21
	v_med3_f32 v27, v27, s59, v189
	v_add_f32_e32 v26, 1.0, v26
	v_add_f32_e32 v31, 1.0, v31
	v_mul_f32_e32 v33, 0x3fd9db23, v21
	v_add_f32_e32 v27, 1.0, v27
	v_mul_f32_e32 v0, v0, v26
	v_mul_f32_e32 v21, v21, v31
	v_add_f32_e32 v26, 1.0, v28
	v_add_f32_e32 v31, 1.0, v150
	v_fmamk_f32 v147, v148, 0x3a800000, v238
	v_mul_f32_e32 v18, v18, v27
	v_add_f32_e32 v27, 1.0, v29
	v_rcp_f32_e32 v26, v26
	v_rcp_f32_e32 v31, v31
	v_fmamk_f32 v19, v159, 0x3a800000, v225
	v_fmamk_f32 v22, v160, 0x3a800000, v226
	v_fmamk_f32 v24, v161, 0x3a800000, v227
	v_med3_f32 v147, v147, s59, v189
	v_rcp_f32_e32 v27, v27
	v_min_f32_e32 v19, 0x40e00000, v19
	v_min_f32_e32 v22, 0x40e00000, v22
	v_min_f32_e32 v24, 0x40e00000, v24
	v_add_f32_e32 v147, 1.0, v147
	v_fmamk_f32 v25, v157, 0x3a800000, v231
	v_mul_f32_e32 v32, 0x3fd9db23, v19
	v_fmamk_f32 v146, v152, 0x3a800000, v234
	v_mul_f32_e32 v148, 0x3fd9db23, v22
	v_mul_f32_e32 v152, 0x3fd9db23, v24
	v_mul_f32_e32 v23, v23, v147
	v_min_f32_e32 v25, 0x40e00000, v25
	v_mul_f32_e32 v32, 0xbfb8aa3b, v32
	v_mul_f32_e32 v148, 0xbfb8aa3b, v148
	v_mul_f32_e32 v0, v0, v26
	v_mul_f32_e32 v26, v23, v31
	v_mul_f32_e32 v23, 0xbfb8aa3b, v152
	v_mul_f32_e32 v33, 0xbfb8aa3b, v33
	v_exp_f32_e32 v32, v32
	v_exp_f32_e32 v148, v148
	v_mul_f32_e32 v18, v18, v27
	v_exp_f32_e32 v23, v23
	v_mul_f32_e32 v27, 0x3fd9db23, v25
	v_fmamk_f32 v30, v151, 0x3a800000, v233
	v_exp_f32_e32 v33, v33
	v_mul_f32_e32 v27, 0xbfb8aa3b, v27
	v_med3_f32 v30, v30, s59, v189
	v_exp_f32_e32 v27, v27
	v_add_f32_e32 v30, 1.0, v30
	v_mul_f32_e32 v19, v19, v30
	v_add_f32_e32 v28, 1.0, v32
	v_add_f32_e32 v30, 1.0, v148
	v_add_f32_e32 v23, 1.0, v23
	v_fmamk_f32 v151, v153, 0x3a800000, v235
	v_add_f32_e32 v29, 1.0, v33
	v_rcp_f32_e32 v28, v28
	v_rcp_f32_e32 v30, v30
	v_rcp_f32_e32 v23, v23
	v_med3_f32 v146, v146, s59, v189
	v_med3_f32 v151, v151, s59, v189
	v_rcp_f32_e32 v29, v29
	v_add_f32_e32 v27, 1.0, v27
	v_fmamk_f32 v149, v149, 0x3a800000, v239
	v_add_f32_e32 v146, 1.0, v146
	v_add_f32_e32 v151, 1.0, v151
	v_rcp_f32_e32 v27, v27
	v_med3_f32 v149, v149, s59, v189
	v_mul_f32_e32 v22, v22, v146
	v_mul_f32_e32 v24, v24, v151
	v_mul_f32_e32 v19, v19, v28
	v_mul_f32_e32 v22, v22, v30
	v_mul_f32_e32 v23, v24, v23
	v_add_f32_e32 v24, 1.0, v149
	v_mul_f32_e32 v21, v21, v29
	v_mul_f32_e32 v24, v25, v24
	v_mul_f32_e32 v0, 4.0, v0
	v_mul_f32_e32 v19, 4.0, v19
	v_mul_f32_e32 v25, 4.0, v22
	v_mov_b32_e32 v22, v171
	v_mul_f32_e32 v24, v24, v27
	v_mul_f32_e32 v27, 4.0, v23
	v_cvt_pk_fp8_f32 v22, v0, v19
	v_mul_f32_e32 v0, 4.0, v18
	v_mul_f32_e32 v18, 4.0, v21
	v_mov_b32_e32 v23, v171
	v_cvt_pk_fp8_f32 v23, v0, v18
	v_mul_f32_e32 v0, 4.0, v26
	v_mul_f32_e32 v18, 4.0, v24
	v_ashrrev_i32_e32 v21, 31, v20
	v_cvt_pk_fp8_f32 v23, v0, v18 op_sel:[0,0,1]
	v_lshlrev_b64 v[18:19], 11, v[20:21]
	v_fmamk_f32 v21, v138, 0x3a800000, v228
	v_cvt_pk_fp8_f32 v22, v25, v27 op_sel:[0,0,1]
	v_min_f32_e32 v21, 0x40e00000, v21
	v_mul_f32_e32 v25, 0x3fd9db23, v21
	v_lshl_add_u64 v[18:19], s[14:15], 0, v[18:19]
	v_mul_f32_e32 v25, 0xbfb8aa3b, v25
	v_lshl_add_u64 v[18:19], v[18:19], 0, v[170:171]
	v_exp_f32_e32 v25, v25
	global_store_dwordx2 v[18:19], v[22:23], off nt
	v_fmamk_f32 v22, v134, 0x3a800000, v232
	v_fmamk_f32 v0, v142, 0x3a800000, v224
	v_med3_f32 v22, v22, s59, v189
	v_min_f32_e32 v0, 0x40e00000, v0
	v_add_f32_e32 v22, 1.0, v22
	v_mul_f32_e32 v24, 0x3fd9db23, v0
	v_mul_f32_e32 v0, v0, v22
	v_add_f32_e32 v22, 1.0, v25
	v_fmamk_f32 v23, v130, 0x3a800000, v236
	v_rcp_f32_e32 v22, v22
	v_med3_f32 v23, v23, s59, v189
	v_mul_f32_e32 v24, 0xbfb8aa3b, v24
	v_exp_f32_e32 v24, v24
	v_add_f32_e32 v23, 1.0, v23
	v_mul_f32_e32 v21, v21, v23
	v_mul_f32_e32 v21, v21, v22
	v_fmamk_f32 v22, v143, 0x3a800000, v225
	v_min_f32_e32 v22, 0x40e00000, v22
	v_add_f32_e32 v24, 1.0, v24
	v_fmamk_f32 v23, v139, 0x3a800000, v229
	v_mul_f32_e32 v26, 0x3fd9db23, v22
	v_rcp_f32_e32 v24, v24
	v_min_f32_e32 v23, 0x40e00000, v23
	v_mul_f32_e32 v26, 0xbfb8aa3b, v26
	v_exp_f32_e32 v26, v26
	v_mul_f32_e32 v27, 0x3fd9db23, v23
	v_mul_f32_e32 v27, 0xbfb8aa3b, v27
	v_exp_f32_e32 v27, v27
	v_mul_f32_e32 v0, v0, v24
	v_fmamk_f32 v24, v135, 0x3a800000, v233
	v_med3_f32 v24, v24, s59, v189
	v_add_f32_e32 v26, 1.0, v26
	v_add_f32_e32 v24, 1.0, v24
	v_rcp_f32_e32 v26, v26
	v_mul_f32_e32 v22, v22, v24
	v_add_f32_e32 v24, 1.0, v27
	v_fmamk_f32 v25, v131, 0x3a800000, v237
	v_rcp_f32_e32 v24, v24
	v_med3_f32 v25, v25, s59, v189
	v_mul_f32_e32 v26, v22, v26
	v_add_f32_e32 v22, 1.0, v25
	v_mul_f32_e32 v22, v23, v22
	v_mul_f32_e32 v23, v22, v24
	v_fmamk_f32 v22, v144, 0x3a800000, v226
	v_min_f32_e32 v22, 0x40e00000, v22
	v_fmamk_f32 v24, v140, 0x3a800000, v230
	v_mul_f32_e32 v28, 0x3fd9db23, v22
	v_min_f32_e32 v24, 0x40e00000, v24
	v_mul_f32_e32 v28, 0xbfb8aa3b, v28
	v_exp_f32_e32 v28, v28
	v_mul_f32_e32 v29, 0x3fd9db23, v24
	v_mul_f32_e32 v29, 0xbfb8aa3b, v29
	v_exp_f32_e32 v29, v29
	v_fmamk_f32 v25, v136, 0x3a800000, v234
	v_med3_f32 v25, v25, s59, v189
	v_add_f32_e32 v28, 1.0, v28
	v_add_f32_e32 v25, 1.0, v25
	v_rcp_f32_e32 v28, v28
	v_mul_f32_e32 v22, v22, v25
	v_add_f32_e32 v25, 1.0, v29
	v_fmamk_f32 v27, v132, 0x3a800000, v238
	v_rcp_f32_e32 v25, v25
	v_med3_f32 v27, v27, s59, v189
	v_mul_f32_e32 v28, v22, v28
	v_add_f32_e32 v22, 1.0, v27
	v_mul_f32_e32 v22, v24, v22
	v_mul_f32_e32 v27, v22, v25
	v_fmamk_f32 v22, v145, 0x3a800000, v227
	v_min_f32_e32 v22, 0x40e00000, v22
	v_fmamk_f32 v24, v141, 0x3a800000, v231
	v_mul_f32_e32 v30, 0x3fd9db23, v22
	v_min_f32_e32 v24, 0x40e00000, v24
	v_mul_f32_e32 v30, 0xbfb8aa3b, v30
	v_exp_f32_e32 v30, v30
	v_mul_f32_e32 v31, 0x3fd9db23, v24
	v_mul_f32_e32 v31, 0xbfb8aa3b, v31
	v_exp_f32_e32 v31, v31
	v_fmamk_f32 v25, v137, 0x3a800000, v235
	v_med3_f32 v25, v25, s59, v189
	v_add_f32_e32 v30, 1.0, v30
	v_add_f32_e32 v25, 1.0, v25
	v_rcp_f32_e32 v30, v30
	v_mul_f32_e32 v22, v22, v25
	v_add_f32_e32 v25, 1.0, v31
	v_fmamk_f32 v29, v133, 0x3a800000, v239
	v_rcp_f32_e32 v25, v25
	v_med3_f32 v29, v29, s59, v189
	v_mul_f32_e32 v30, v22, v30
	v_add_f32_e32 v22, 1.0, v29
	v_mul_f32_e32 v22, v24, v22
	v_mul_f32_e32 v29, v22, v25
	v_mul_f32_e32 v0, 4.0, v0
	v_mul_f32_e32 v25, 4.0, v26
	v_mov_b32_e32 v24, v171
	v_cvt_pk_fp8_f32 v24, v0, v25
	v_mul_f32_e32 v0, 4.0, v21
	v_mul_f32_e32 v21, 4.0, v23
	v_mov_b32_e32 v25, v171
	v_cvt_pk_fp8_f32 v25, v0, v21
	v_or_b32_e32 v22, 16, v20
	v_mul_f32_e32 v26, 4.0, v28
	v_mul_f32_e32 v28, 4.0, v30
	v_mul_f32_e32 v0, 4.0, v27
	v_mul_f32_e32 v21, 4.0, v29
	v_cvt_pk_fp8_f32 v24, v26, v28 op_sel:[0,0,1]
	v_cvt_pk_fp8_f32 v25, v0, v21 op_sel:[0,0,1]
	v_ashrrev_i32_e32 v23, 31, v22
	v_lshlrev_b64 v[22:23], 11, v[22:23]
	v_lshl_add_u64 v[22:23], s[14:15], 0, v[22:23]
	v_fmamk_f32 v21, v122, 0x3a800000, v228
	v_lshl_add_u64 v[22:23], v[22:23], 0, v[170:171]
	v_min_f32_e32 v21, 0x40e00000, v21
	global_store_dwordx2 v[22:23], v[24:25], off nt
	v_mul_f32_e32 v25, 0x3fd9db23, v21
	v_mul_f32_e32 v25, 0xbfb8aa3b, v25
	v_exp_f32_e32 v25, v25
	v_fmamk_f32 v22, v118, 0x3a800000, v232
	v_fmamk_f32 v0, v126, 0x3a800000, v224
	v_med3_f32 v22, v22, s59, v189
	v_min_f32_e32 v0, 0x40e00000, v0
	v_add_f32_e32 v22, 1.0, v22
	v_mul_f32_e32 v24, 0x3fd9db23, v0
	v_mul_f32_e32 v0, v0, v22
	v_add_f32_e32 v22, 1.0, v25
	v_fmamk_f32 v23, v114, 0x3a800000, v236
	v_rcp_f32_e32 v22, v22
	v_med3_f32 v23, v23, s59, v189
	v_mul_f32_e32 v24, 0xbfb8aa3b, v24
	v_exp_f32_e32 v24, v24
	v_add_f32_e32 v23, 1.0, v23
	v_mul_f32_e32 v21, v21, v23
	v_mul_f32_e32 v21, v21, v22
	v_fmamk_f32 v22, v127, 0x3a800000, v225
	v_min_f32_e32 v22, 0x40e00000, v22
	v_add_f32_e32 v24, 1.0, v24
	v_fmamk_f32 v23, v123, 0x3a800000, v229
	v_mul_f32_e32 v26, 0x3fd9db23, v22
	v_rcp_f32_e32 v24, v24
	v_min_f32_e32 v23, 0x40e00000, v23
	v_mul_f32_e32 v26, 0xbfb8aa3b, v26
	v_exp_f32_e32 v26, v26
	v_mul_f32_e32 v27, 0x3fd9db23, v23
	v_mul_f32_e32 v27, 0xbfb8aa3b, v27
	v_exp_f32_e32 v27, v27
	v_mul_f32_e32 v0, v0, v24
	v_fmamk_f32 v24, v119, 0x3a800000, v233
	v_med3_f32 v24, v24, s59, v189
	v_add_f32_e32 v26, 1.0, v26
	v_add_f32_e32 v24, 1.0, v24
	v_rcp_f32_e32 v26, v26
	v_mul_f32_e32 v22, v22, v24
	v_add_f32_e32 v24, 1.0, v27
	v_fmamk_f32 v25, v115, 0x3a800000, v237
	v_rcp_f32_e32 v24, v24
	v_med3_f32 v25, v25, s59, v189
	v_mul_f32_e32 v26, v22, v26
	v_add_f32_e32 v22, 1.0, v25
	v_mul_f32_e32 v22, v23, v22
	v_mul_f32_e32 v23, v22, v24
	v_fmamk_f32 v22, v128, 0x3a800000, v226
	v_min_f32_e32 v22, 0x40e00000, v22
	v_fmamk_f32 v24, v124, 0x3a800000, v230
	v_mul_f32_e32 v28, 0x3fd9db23, v22
	v_min_f32_e32 v24, 0x40e00000, v24
	v_mul_f32_e32 v28, 0xbfb8aa3b, v28
	v_exp_f32_e32 v28, v28
	v_mul_f32_e32 v29, 0x3fd9db23, v24
	v_mul_f32_e32 v29, 0xbfb8aa3b, v29
	v_exp_f32_e32 v29, v29
	v_fmamk_f32 v25, v120, 0x3a800000, v234
	v_med3_f32 v25, v25, s59, v189
	v_add_f32_e32 v28, 1.0, v28
	v_add_f32_e32 v25, 1.0, v25
	v_rcp_f32_e32 v28, v28
	v_mul_f32_e32 v22, v22, v25
	v_add_f32_e32 v25, 1.0, v29
	v_fmamk_f32 v27, v116, 0x3a800000, v238
	v_rcp_f32_e32 v25, v25
	v_med3_f32 v27, v27, s59, v189
	v_mul_f32_e32 v28, v22, v28
	v_add_f32_e32 v22, 1.0, v27
	v_mul_f32_e32 v22, v24, v22
	v_mul_f32_e32 v27, v22, v25
	v_fmamk_f32 v22, v129, 0x3a800000, v227
	v_min_f32_e32 v22, 0x40e00000, v22
	v_fmamk_f32 v24, v125, 0x3a800000, v231
	v_mul_f32_e32 v30, 0x3fd9db23, v22
	v_min_f32_e32 v24, 0x40e00000, v24
	v_mul_f32_e32 v30, 0xbfb8aa3b, v30
	v_exp_f32_e32 v30, v30
	v_mul_f32_e32 v31, 0x3fd9db23, v24
	v_mul_f32_e32 v31, 0xbfb8aa3b, v31
	v_exp_f32_e32 v31, v31
	v_fmamk_f32 v25, v121, 0x3a800000, v235
	v_med3_f32 v25, v25, s59, v189
	v_add_f32_e32 v30, 1.0, v30
	v_add_f32_e32 v25, 1.0, v25
	v_rcp_f32_e32 v30, v30
	v_mul_f32_e32 v22, v22, v25
	v_add_f32_e32 v25, 1.0, v31
	v_fmamk_f32 v29, v117, 0x3a800000, v239
	v_rcp_f32_e32 v25, v25
	v_med3_f32 v29, v29, s59, v189
	v_mul_f32_e32 v30, v22, v30
	v_add_f32_e32 v22, 1.0, v29
	v_mul_f32_e32 v22, v24, v22
	v_mul_f32_e32 v29, v22, v25
	v_mul_f32_e32 v0, 4.0, v0
	v_mul_f32_e32 v25, 4.0, v26
	v_mov_b32_e32 v24, v171
	v_cvt_pk_fp8_f32 v24, v0, v25
	v_mul_f32_e32 v0, 4.0, v21
	v_mul_f32_e32 v21, 4.0, v23
	v_mov_b32_e32 v25, v171
	v_cvt_pk_fp8_f32 v25, v0, v21
	v_or_b32_e32 v22, 32, v20
	v_mul_f32_e32 v26, 4.0, v28
	v_mul_f32_e32 v28, 4.0, v30
	v_mul_f32_e32 v0, 4.0, v27
	v_mul_f32_e32 v21, 4.0, v29
	v_cvt_pk_fp8_f32 v24, v26, v28 op_sel:[0,0,1]
	v_cvt_pk_fp8_f32 v25, v0, v21 op_sel:[0,0,1]
	v_ashrrev_i32_e32 v23, 31, v22
	v_lshlrev_b64 v[22:23], 11, v[22:23]
	v_lshl_add_u64 v[22:23], s[14:15], 0, v[22:23]
	v_fmamk_f32 v21, v106, 0x3a800000, v228
	v_lshl_add_u64 v[22:23], v[22:23], 0, v[170:171]
	v_fmamk_f32 v0, v110, 0x3a800000, v224
	v_min_f32_e32 v21, 0x40e00000, v21
	global_store_dwordx2 v[22:23], v[24:25], off nt
	v_min_f32_e32 v0, 0x40e00000, v0
	v_mul_f32_e32 v25, 0x3fd9db23, v21
	v_mul_f32_e32 v24, 0x3fd9db23, v0
	v_mul_f32_e32 v25, 0xbfb8aa3b, v25
	v_mul_f32_e32 v24, 0xbfb8aa3b, v24
	v_exp_f32_e32 v25, v25
	v_fmamk_f32 v22, v102, 0x3a800000, v232
	v_exp_f32_e32 v24, v24
	v_med3_f32 v22, v22, s59, v189
	v_fmamk_f32 v23, v98, 0x3a800000, v236
	v_med3_f32 v23, v23, s59, v189
	v_add_f32_e32 v22, 1.0, v22
	v_mul_f32_e32 v0, v0, v22
	v_add_f32_e32 v22, 1.0, v25
	v_add_f32_e32 v23, 1.0, v23
	v_add_f32_e32 v24, 1.0, v24
	v_rcp_f32_e32 v22, v22
	v_mul_f32_e32 v21, v21, v23
	v_fmamk_f32 v23, v107, 0x3a800000, v229
	v_rcp_f32_e32 v24, v24
	v_min_f32_e32 v23, 0x40e00000, v23
	v_mul_f32_e32 v27, 0x3fd9db23, v23
	v_mul_f32_e32 v27, 0xbfb8aa3b, v27
	v_mul_f32_e32 v21, v21, v22
	v_fmamk_f32 v22, v111, 0x3a800000, v225
	v_exp_f32_e32 v27, v27
	v_mul_f32_e32 v0, v0, v24
	v_min_f32_e32 v22, 0x40e00000, v22
	v_fmamk_f32 v24, v103, 0x3a800000, v233
	v_med3_f32 v24, v24, s59, v189
	v_mul_f32_e32 v26, 0x3fd9db23, v22
	v_add_f32_e32 v24, 1.0, v24
	v_mul_f32_e32 v26, 0xbfb8aa3b, v26
	v_exp_f32_e32 v26, v26
	v_mul_f32_e32 v22, v22, v24
	v_add_f32_e32 v24, 1.0, v27
	v_fmamk_f32 v25, v99, 0x3a800000, v237
	v_rcp_f32_e32 v24, v24
	v_med3_f32 v25, v25, s59, v189
	v_add_f32_e32 v25, 1.0, v25
	v_add_f32_e32 v26, 1.0, v26
	v_mul_f32_e32 v23, v23, v25
	v_fmamk_f32 v25, v108, 0x3a800000, v230
	v_rcp_f32_e32 v26, v26
	v_mul_f32_e32 v23, v23, v24
	v_fmamk_f32 v24, v112, 0x3a800000, v226
	v_min_f32_e32 v25, 0x40e00000, v25
	v_min_f32_e32 v24, 0x40e00000, v24
	v_mul_f32_e32 v29, 0x3fd9db23, v25
	v_mul_f32_e32 v28, 0x3fd9db23, v24
	v_mul_f32_e32 v29, 0xbfb8aa3b, v29
	v_mul_f32_e32 v28, 0xbfb8aa3b, v28
	v_exp_f32_e32 v29, v29
	v_mul_f32_e32 v22, v22, v26
	v_fmamk_f32 v26, v104, 0x3a800000, v234
	v_exp_f32_e32 v28, v28
	v_med3_f32 v26, v26, s59, v189
	v_fmamk_f32 v27, v100, 0x3a800000, v238
	v_med3_f32 v27, v27, s59, v189
	v_add_f32_e32 v26, 1.0, v26
	v_mul_f32_e32 v24, v24, v26
	v_add_f32_e32 v26, 1.0, v29
	v_add_f32_e32 v27, 1.0, v27
	v_add_f32_e32 v28, 1.0, v28
	v_rcp_f32_e32 v26, v26
	v_mul_f32_e32 v25, v25, v27
	v_fmamk_f32 v27, v109, 0x3a800000, v231
	v_rcp_f32_e32 v28, v28
	v_min_f32_e32 v27, 0x40e00000, v27
	v_mul_f32_e32 v31, 0x3fd9db23, v27
	v_mul_f32_e32 v31, 0xbfb8aa3b, v31
	v_mul_f32_e32 v25, v25, v26
	v_fmamk_f32 v26, v113, 0x3a800000, v227
	v_exp_f32_e32 v31, v31
	v_mul_f32_e32 v24, v24, v28
	v_min_f32_e32 v26, 0x40e00000, v26
	v_fmamk_f32 v28, v105, 0x3a800000, v235
	v_med3_f32 v28, v28, s59, v189
	v_mul_f32_e32 v30, 0x3fd9db23, v26
	v_add_f32_e32 v28, 1.0, v28
	v_mul_f32_e32 v30, 0xbfb8aa3b, v30
	v_exp_f32_e32 v30, v30
	v_mul_f32_e32 v26, v26, v28
	v_add_f32_e32 v28, 1.0, v31
	v_fmamk_f32 v29, v101, 0x3a800000, v239
	v_rcp_f32_e32 v28, v28
	v_med3_f32 v29, v29, s59, v189
	v_add_f32_e32 v29, 1.0, v29
	v_add_f32_e32 v30, 1.0, v30
	v_mul_f32_e32 v27, v27, v29
	v_rcp_f32_e32 v30, v30
	v_mul_f32_e32 v27, v27, v28
	v_mul_f32_e32 v0, 4.0, v0
	v_mul_f32_e32 v28, 4.0, v22
	v_mov_b32_e32 v22, v171
	v_cvt_pk_fp8_f32 v22, v0, v28
	v_mul_f32_e32 v0, 4.0, v21
	v_mul_f32_e32 v21, 4.0, v23
	v_mov_b32_e32 v23, v171
	v_cvt_pk_fp8_f32 v23, v0, v21
	v_mul_f32_e32 v26, v26, v30
	v_or_b32_e32 v20, 48, v20
	v_mul_f32_e32 v24, 4.0, v24
	v_mul_f32_e32 v26, 4.0, v26
	v_mul_f32_e32 v0, 4.0, v25
	v_mul_f32_e32 v21, 4.0, v27
	v_cvt_pk_fp8_f32 v22, v24, v26 op_sel:[0,0,1]
	v_cvt_pk_fp8_f32 v23, v0, v21 op_sel:[0,0,1]
	v_ashrrev_i32_e32 v21, 31, v20
	v_lshlrev_b64 v[20:21], 11, v[20:21]
	v_lshl_add_u64 v[20:21], s[14:15], 0, v[20:21]
	v_lshl_add_u64 v[20:21], v[20:21], 0, v[170:171]
	global_store_dwordx2 v[20:21], v[22:23], off nt
	v_fmamk_f32 v20, v90, 0x3a800000, v228
	v_fmamk_f32 v0, v94, 0x3a800000, v224
	v_min_f32_e32 v20, 0x40e00000, v20
	v_min_f32_e32 v0, 0x40e00000, v0
	v_mul_f32_e32 v24, 0x3fd9db23, v20
	v_mul_f32_e32 v23, 0x3fd9db23, v0
	v_mul_f32_e32 v24, 0xbfb8aa3b, v24
	v_mul_f32_e32 v23, 0xbfb8aa3b, v23
	v_exp_f32_e32 v24, v24
	v_fmamk_f32 v21, v86, 0x3a800000, v232
	v_exp_f32_e32 v23, v23
	v_med3_f32 v21, v21, s59, v189
	v_fmamk_f32 v22, v82, 0x3a800000, v236
	v_med3_f32 v22, v22, s59, v189
	v_add_f32_e32 v21, 1.0, v21
	v_mul_f32_e32 v0, v0, v21
	v_add_f32_e32 v21, 1.0, v24
	v_add_f32_e32 v22, 1.0, v22
	v_add_f32_e32 v23, 1.0, v23
	v_rcp_f32_e32 v21, v21
	v_mul_f32_e32 v20, v20, v22
	v_fmamk_f32 v22, v91, 0x3a800000, v229
	v_rcp_f32_e32 v23, v23
	v_min_f32_e32 v22, 0x40e00000, v22
	v_mul_f32_e32 v26, 0x3fd9db23, v22
	v_mul_f32_e32 v26, 0xbfb8aa3b, v26
	v_mul_f32_e32 v21, v20, v21
	v_fmamk_f32 v20, v95, 0x3a800000, v225
	v_exp_f32_e32 v26, v26
	v_mul_f32_e32 v0, v0, v23
	v_min_f32_e32 v20, 0x40e00000, v20
	v_fmamk_f32 v23, v87, 0x3a800000, v233
	v_med3_f32 v23, v23, s59, v189
	v_mul_f32_e32 v25, 0x3fd9db23, v20
	v_add_f32_e32 v23, 1.0, v23
	v_mul_f32_e32 v25, 0xbfb8aa3b, v25
	v_exp_f32_e32 v25, v25
	v_mul_f32_e32 v20, v20, v23
	v_add_f32_e32 v23, 1.0, v26
	v_fmamk_f32 v24, v83, 0x3a800000, v237
	v_rcp_f32_e32 v23, v23
	v_med3_f32 v24, v24, s59, v189
	v_add_f32_e32 v24, 1.0, v24
	v_add_f32_e32 v25, 1.0, v25
	v_mul_f32_e32 v22, v22, v24
	v_fmamk_f32 v24, v92, 0x3a800000, v230
	v_rcp_f32_e32 v25, v25
	v_mul_f32_e32 v22, v22, v23
	v_fmamk_f32 v23, v96, 0x3a800000, v226
	v_min_f32_e32 v24, 0x40e00000, v24
	v_min_f32_e32 v23, 0x40e00000, v23
	v_mul_f32_e32 v28, 0x3fd9db23, v24
	v_mul_f32_e32 v27, 0x3fd9db23, v23
	v_mul_f32_e32 v28, 0xbfb8aa3b, v28
	v_mul_f32_e32 v27, 0xbfb8aa3b, v27
	v_exp_f32_e32 v28, v28
	v_mul_f32_e32 v20, v20, v25
	v_fmamk_f32 v25, v88, 0x3a800000, v234
	v_exp_f32_e32 v27, v27
	v_med3_f32 v25, v25, s59, v189
	v_fmamk_f32 v26, v84, 0x3a800000, v238
	v_med3_f32 v26, v26, s59, v189
	v_add_f32_e32 v25, 1.0, v25
	v_mul_f32_e32 v23, v23, v25
	v_add_f32_e32 v25, 1.0, v28
	v_add_f32_e32 v26, 1.0, v26
	v_add_f32_e32 v27, 1.0, v27
	v_rcp_f32_e32 v25, v25
	v_mul_f32_e32 v24, v24, v26
	v_fmamk_f32 v26, v93, 0x3a800000, v231
	v_rcp_f32_e32 v27, v27
	v_min_f32_e32 v26, 0x40e00000, v26
	v_mul_f32_e32 v30, 0x3fd9db23, v26
	v_mul_f32_e32 v30, 0xbfb8aa3b, v30
	v_mul_f32_e32 v24, v24, v25
	v_fmamk_f32 v25, v97, 0x3a800000, v227
	v_exp_f32_e32 v30, v30
	v_mul_f32_e32 v23, v23, v27
	v_min_f32_e32 v25, 0x40e00000, v25
	v_fmamk_f32 v27, v89, 0x3a800000, v235
	v_med3_f32 v27, v27, s59, v189
	v_mul_f32_e32 v29, 0x3fd9db23, v25
	v_add_f32_e32 v27, 1.0, v27
	v_mul_f32_e32 v29, 0xbfb8aa3b, v29
	v_exp_f32_e32 v29, v29
	v_mul_f32_e32 v25, v25, v27
	v_add_f32_e32 v27, 1.0, v30
	v_fmamk_f32 v28, v85, 0x3a800000, v239
	v_rcp_f32_e32 v27, v27
	v_med3_f32 v28, v28, s59, v189
	v_add_f32_e32 v28, 1.0, v28
	v_add_f32_e32 v29, 1.0, v29
	v_mul_f32_e32 v26, v26, v28
	v_rcp_f32_e32 v29, v29
	v_mul_f32_e32 v26, v26, v27
	v_mul_f32_e32 v0, 4.0, v0
	v_mul_f32_e32 v27, 4.0, v20
	v_mov_b32_e32 v20, v171
	v_cvt_pk_fp8_f32 v20, v0, v27
	v_mul_f32_e32 v0, 4.0, v21
	v_mul_f32_e32 v22, 4.0, v22
	v_mov_b32_e32 v21, v171
	v_cvt_pk_fp8_f32 v21, v0, v22
	v_mul_f32_e32 v25, v25, v29
	v_mul_f32_e32 v23, 4.0, v23
	v_mul_f32_e32 v25, 4.0, v25
	v_mul_f32_e32 v0, 4.0, v24
	v_mul_f32_e32 v22, 4.0, v26
	v_cvt_pk_fp8_f32 v20, v23, v25 op_sel:[0,0,1]
	v_cvt_pk_fp8_f32 v21, v0, v22 op_sel:[0,0,1]
	v_add_co_u32_e32 v22, vcc, s60, v18
	v_fmamk_f32 v0, v78, 0x3a800000, v224
	s_nop 0
	v_addc_co_u32_e32 v23, vcc, 0, v19, vcc
	global_store_dwordx2 v[22:23], v[20:21], off nt
	v_fmamk_f32 v20, v74, 0x3a800000, v228
	v_min_f32_e32 v20, 0x40e00000, v20
	v_min_f32_e32 v0, 0x40e00000, v0
	v_mul_f32_e32 v24, 0x3fd9db23, v20
	v_mul_f32_e32 v23, 0x3fd9db23, v0
	v_mul_f32_e32 v24, 0xbfb8aa3b, v24
	v_mul_f32_e32 v23, 0xbfb8aa3b, v23
	v_exp_f32_e32 v24, v24
	v_fmamk_f32 v21, v70, 0x3a800000, v232
	v_exp_f32_e32 v23, v23
	v_med3_f32 v21, v21, s59, v189
	v_fmamk_f32 v22, v66, 0x3a800000, v236
	v_med3_f32 v22, v22, s59, v189
	v_add_f32_e32 v21, 1.0, v21
	v_mul_f32_e32 v0, v0, v21
	v_add_f32_e32 v21, 1.0, v24
	v_add_f32_e32 v22, 1.0, v22
	v_add_f32_e32 v23, 1.0, v23
	v_rcp_f32_e32 v21, v21
	v_mul_f32_e32 v20, v20, v22
	v_fmamk_f32 v22, v75, 0x3a800000, v229
	v_rcp_f32_e32 v23, v23
	v_min_f32_e32 v22, 0x40e00000, v22
	v_mul_f32_e32 v26, 0x3fd9db23, v22
	v_mul_f32_e32 v26, 0xbfb8aa3b, v26
	v_mul_f32_e32 v21, v20, v21
	v_fmamk_f32 v20, v79, 0x3a800000, v225
	v_exp_f32_e32 v26, v26
	v_mul_f32_e32 v0, v0, v23
	v_min_f32_e32 v20, 0x40e00000, v20
	v_fmamk_f32 v23, v71, 0x3a800000, v233
	v_med3_f32 v23, v23, s59, v189
	v_mul_f32_e32 v25, 0x3fd9db23, v20
	v_add_f32_e32 v23, 1.0, v23
	v_mul_f32_e32 v25, 0xbfb8aa3b, v25
	v_exp_f32_e32 v25, v25
	v_mul_f32_e32 v20, v20, v23
	v_add_f32_e32 v23, 1.0, v26
	v_fmamk_f32 v24, v67, 0x3a800000, v237
	v_rcp_f32_e32 v23, v23
	v_med3_f32 v24, v24, s59, v189
	v_add_f32_e32 v24, 1.0, v24
	v_add_f32_e32 v25, 1.0, v25
	v_mul_f32_e32 v22, v22, v24
	v_fmamk_f32 v24, v76, 0x3a800000, v230
	v_rcp_f32_e32 v25, v25
	v_mul_f32_e32 v22, v22, v23
	v_fmamk_f32 v23, v80, 0x3a800000, v226
	v_min_f32_e32 v24, 0x40e00000, v24
	v_min_f32_e32 v23, 0x40e00000, v23
	v_mul_f32_e32 v28, 0x3fd9db23, v24
	v_mul_f32_e32 v27, 0x3fd9db23, v23
	v_mul_f32_e32 v28, 0xbfb8aa3b, v28
	v_mul_f32_e32 v27, 0xbfb8aa3b, v27
	v_exp_f32_e32 v28, v28
	v_mul_f32_e32 v20, v20, v25
	v_fmamk_f32 v25, v72, 0x3a800000, v234
	v_exp_f32_e32 v27, v27
	v_med3_f32 v25, v25, s59, v189
	v_fmamk_f32 v26, v68, 0x3a800000, v238
	v_med3_f32 v26, v26, s59, v189
	v_add_f32_e32 v25, 1.0, v25
	v_mul_f32_e32 v23, v23, v25
	v_add_f32_e32 v25, 1.0, v28
	v_add_f32_e32 v26, 1.0, v26
	v_add_f32_e32 v27, 1.0, v27
	v_rcp_f32_e32 v25, v25
	v_mul_f32_e32 v24, v24, v26
	v_fmamk_f32 v26, v77, 0x3a800000, v231
	v_rcp_f32_e32 v27, v27
	v_min_f32_e32 v26, 0x40e00000, v26
	v_mul_f32_e32 v30, 0x3fd9db23, v26
	v_mul_f32_e32 v30, 0xbfb8aa3b, v30
	v_mul_f32_e32 v24, v24, v25
	v_fmamk_f32 v25, v81, 0x3a800000, v227
	v_exp_f32_e32 v30, v30
	v_mul_f32_e32 v23, v23, v27
	v_min_f32_e32 v25, 0x40e00000, v25
	v_fmamk_f32 v27, v73, 0x3a800000, v235
	v_med3_f32 v27, v27, s59, v189
	v_mul_f32_e32 v29, 0x3fd9db23, v25
	v_add_f32_e32 v27, 1.0, v27
	v_mul_f32_e32 v29, 0xbfb8aa3b, v29
	v_exp_f32_e32 v29, v29
	v_mul_f32_e32 v25, v25, v27
	v_add_f32_e32 v27, 1.0, v30
	v_fmamk_f32 v28, v69, 0x3a800000, v239
	v_rcp_f32_e32 v27, v27
	v_med3_f32 v28, v28, s59, v189
	v_add_f32_e32 v28, 1.0, v28
	v_add_f32_e32 v29, 1.0, v29
	v_mul_f32_e32 v26, v26, v28
	v_rcp_f32_e32 v29, v29
	v_mul_f32_e32 v26, v26, v27
	v_mul_f32_e32 v0, 4.0, v0
	v_mul_f32_e32 v27, 4.0, v20
	v_mov_b32_e32 v20, v171
	v_cvt_pk_fp8_f32 v20, v0, v27
	v_mul_f32_e32 v0, 4.0, v21
	v_mul_f32_e32 v22, 4.0, v22
	v_mov_b32_e32 v21, v171
	v_cvt_pk_fp8_f32 v21, v0, v22
	v_mul_f32_e32 v25, v25, v29
	v_mul_f32_e32 v23, 4.0, v23
	v_mul_f32_e32 v25, 4.0, v25
	v_mul_f32_e32 v0, 4.0, v24
	v_mul_f32_e32 v22, 4.0, v26
	v_cvt_pk_fp8_f32 v20, v23, v25 op_sel:[0,0,1]
	v_cvt_pk_fp8_f32 v21, v0, v22 op_sel:[0,0,1]
	v_add_co_u32_e32 v22, vcc, s61, v18
	v_fmamk_f32 v0, v62, 0x3a800000, v224
	s_nop 0
	v_addc_co_u32_e32 v23, vcc, 0, v19, vcc
	global_store_dwordx2 v[22:23], v[20:21], off nt
	v_fmamk_f32 v20, v58, 0x3a800000, v228
	v_min_f32_e32 v20, 0x40e00000, v20
	v_min_f32_e32 v0, 0x40e00000, v0
	v_mul_f32_e32 v24, 0x3fd9db23, v20
	v_mul_f32_e32 v23, 0x3fd9db23, v0
	v_mul_f32_e32 v24, 0xbfb8aa3b, v24
	v_mul_f32_e32 v23, 0xbfb8aa3b, v23
	v_exp_f32_e32 v24, v24
	v_fmamk_f32 v21, v54, 0x3a800000, v232
	v_exp_f32_e32 v23, v23
	v_med3_f32 v21, v21, s59, v189
	v_fmamk_f32 v22, v50, 0x3a800000, v236
	v_med3_f32 v22, v22, s59, v189
	v_add_f32_e32 v21, 1.0, v21
	v_mul_f32_e32 v0, v0, v21
	v_add_f32_e32 v21, 1.0, v24
	v_add_f32_e32 v22, 1.0, v22
	v_add_f32_e32 v23, 1.0, v23
	v_rcp_f32_e32 v21, v21
	v_mul_f32_e32 v20, v20, v22
	v_fmamk_f32 v22, v59, 0x3a800000, v229
	v_rcp_f32_e32 v23, v23
	v_min_f32_e32 v22, 0x40e00000, v22
	v_mul_f32_e32 v26, 0x3fd9db23, v22
	v_mul_f32_e32 v26, 0xbfb8aa3b, v26
	v_mul_f32_e32 v21, v20, v21
	v_fmamk_f32 v20, v63, 0x3a800000, v225
	v_exp_f32_e32 v26, v26
	v_mul_f32_e32 v0, v0, v23
	v_min_f32_e32 v20, 0x40e00000, v20
	v_fmamk_f32 v23, v55, 0x3a800000, v233
	v_med3_f32 v23, v23, s59, v189
	v_mul_f32_e32 v25, 0x3fd9db23, v20
	v_add_f32_e32 v23, 1.0, v23
	v_mul_f32_e32 v25, 0xbfb8aa3b, v25
	v_exp_f32_e32 v25, v25
	v_mul_f32_e32 v20, v20, v23
	v_add_f32_e32 v23, 1.0, v26
	v_fmamk_f32 v24, v51, 0x3a800000, v237
	v_rcp_f32_e32 v23, v23
	v_med3_f32 v24, v24, s59, v189
	v_add_f32_e32 v24, 1.0, v24
	v_add_f32_e32 v25, 1.0, v25
	v_mul_f32_e32 v22, v22, v24
	v_fmamk_f32 v24, v60, 0x3a800000, v230
	v_rcp_f32_e32 v25, v25
	v_mul_f32_e32 v22, v22, v23
	v_fmamk_f32 v23, v64, 0x3a800000, v226
	v_min_f32_e32 v24, 0x40e00000, v24
	v_min_f32_e32 v23, 0x40e00000, v23
	v_mul_f32_e32 v28, 0x3fd9db23, v24
	v_mul_f32_e32 v27, 0x3fd9db23, v23
	v_mul_f32_e32 v28, 0xbfb8aa3b, v28
	v_mul_f32_e32 v27, 0xbfb8aa3b, v27
	v_exp_f32_e32 v28, v28
	v_mul_f32_e32 v20, v20, v25
	v_fmamk_f32 v25, v56, 0x3a800000, v234
	v_exp_f32_e32 v27, v27
	v_med3_f32 v25, v25, s59, v189
	v_fmamk_f32 v26, v52, 0x3a800000, v238
	v_med3_f32 v26, v26, s59, v189
	v_add_f32_e32 v25, 1.0, v25
	v_mul_f32_e32 v23, v23, v25
	v_add_f32_e32 v25, 1.0, v28
	v_add_f32_e32 v26, 1.0, v26
	v_add_f32_e32 v27, 1.0, v27
	v_rcp_f32_e32 v25, v25
	v_mul_f32_e32 v24, v24, v26
	v_fmamk_f32 v26, v61, 0x3a800000, v231
	v_rcp_f32_e32 v27, v27
	v_min_f32_e32 v26, 0x40e00000, v26
	v_mul_f32_e32 v30, 0x3fd9db23, v26
	v_mul_f32_e32 v30, 0xbfb8aa3b, v30
	v_mul_f32_e32 v24, v24, v25
	v_fmamk_f32 v25, v65, 0x3a800000, v227
	v_exp_f32_e32 v30, v30
	v_mul_f32_e32 v23, v23, v27
	v_min_f32_e32 v25, 0x40e00000, v25
	v_fmamk_f32 v27, v57, 0x3a800000, v235
	v_med3_f32 v27, v27, s59, v189
	v_mul_f32_e32 v29, 0x3fd9db23, v25
	v_add_f32_e32 v27, 1.0, v27
	v_mul_f32_e32 v29, 0xbfb8aa3b, v29
	v_exp_f32_e32 v29, v29
	v_mul_f32_e32 v25, v25, v27
	v_add_f32_e32 v27, 1.0, v30
	v_fmamk_f32 v28, v53, 0x3a800000, v239
	v_rcp_f32_e32 v27, v27
	v_med3_f32 v28, v28, s59, v189
	v_add_f32_e32 v28, 1.0, v28
	v_add_f32_e32 v29, 1.0, v29
	v_mul_f32_e32 v26, v26, v28
	v_rcp_f32_e32 v29, v29
	v_mul_f32_e32 v26, v26, v27
	v_mul_f32_e32 v0, 4.0, v0
	v_mul_f32_e32 v27, 4.0, v20
	v_mov_b32_e32 v20, v171
	v_cvt_pk_fp8_f32 v20, v0, v27
	v_mul_f32_e32 v0, 4.0, v21
	v_mul_f32_e32 v22, 4.0, v22
	v_mov_b32_e32 v21, v171
	v_cvt_pk_fp8_f32 v21, v0, v22
	v_mul_f32_e32 v25, v25, v29
	v_mul_f32_e32 v23, 4.0, v23
	v_mul_f32_e32 v25, 4.0, v25
	v_mul_f32_e32 v0, 4.0, v24
	v_mul_f32_e32 v22, 4.0, v26
	v_cvt_pk_fp8_f32 v20, v23, v25 op_sel:[0,0,1]
	v_cvt_pk_fp8_f32 v21, v0, v22 op_sel:[0,0,1]
	v_add_co_u32_e32 v22, vcc, s62, v18
	v_fmamk_f32 v2, v42, 0x3a800000, v228
	s_nop 0
	v_addc_co_u32_e32 v23, vcc, 0, v19, vcc
	v_min_f32_e32 v2, 0x40e00000, v2
	global_store_dwordx2 v[22:23], v[20:21], off nt
	v_mul_f32_e32 v20, 0x3fd9db23, v2
	v_mul_f32_e32 v20, 0xbfb8aa3b, v20
	v_exp_f32_e32 v20, v20
	v_fmamk_f32 v0, v46, 0x3a800000, v224
	v_fmamk_f32 v10, v38, 0x3a800000, v232
	v_med3_f32 v10, v10, s59, v189
	v_min_f32_e32 v0, 0x40e00000, v0
	v_add_f32_e32 v10, 1.0, v10
	v_mul_f32_e32 v14, 0x3fd9db23, v0
	v_mul_f32_e32 v0, v0, v10
	v_add_f32_e32 v10, 1.0, v20
	v_fmamk_f32 v6, v34, 0x3a800000, v236
	v_rcp_f32_e32 v10, v10
	v_med3_f32 v6, v6, s59, v189
	v_add_f32_e32 v6, 1.0, v6
	v_mul_f32_e32 v14, 0xbfb8aa3b, v14
	v_mul_f32_e32 v2, v2, v6
	v_exp_f32_e32 v14, v14
	v_mul_f32_e32 v6, v2, v10
	v_fmamk_f32 v2, v47, 0x3a800000, v225
	v_min_f32_e32 v2, 0x40e00000, v2
	v_mul_f32_e32 v11, 0x3fd9db23, v2
	v_mul_f32_e32 v11, 0xbfb8aa3b, v11
	v_add_f32_e32 v14, 1.0, v14
	v_exp_f32_e32 v11, v11
	v_rcp_f32_e32 v14, v14
	v_fmamk_f32 v3, v43, 0x3a800000, v229
	v_min_f32_e32 v3, 0x40e00000, v3
	v_fmamk_f32 v7, v35, 0x3a800000, v237
	v_add_f32_e32 v11, 1.0, v11
	v_mul_f32_e32 v0, v0, v14
	v_fmamk_f32 v10, v39, 0x3a800000, v233
	v_med3_f32 v7, v7, s59, v189
	v_mul_f32_e32 v14, 0x3fd9db23, v3
	v_rcp_f32_e32 v11, v11
	v_med3_f32 v10, v10, s59, v189
	v_mul_f32_e32 v14, 0xbfb8aa3b, v14
	v_add_f32_e32 v7, 1.0, v7
	v_add_f32_e32 v10, 1.0, v10
	v_exp_f32_e32 v14, v14
	v_mul_f32_e32 v3, v3, v7
	v_fmamk_f32 v7, v48, 0x3a800000, v226
	v_mul_f32_e32 v2, v2, v10
	v_min_f32_e32 v7, 0x40e00000, v7
	v_mul_f32_e32 v2, v2, v11
	v_mul_f32_e32 v11, 0x3fd9db23, v7
	v_mul_f32_e32 v11, 0xbfb8aa3b, v11
	v_add_f32_e32 v10, 1.0, v14
	v_fmamk_f32 v4, v44, 0x3a800000, v230
	v_exp_f32_e32 v11, v11
	v_rcp_f32_e32 v10, v10
	v_min_f32_e32 v4, 0x40e00000, v4
	v_mul_f32_e32 v12, 0x3fd9db23, v4
	v_mul_f32_e32 v12, 0xbfb8aa3b, v12
	v_exp_f32_e32 v12, v12
	v_add_f32_e32 v11, 1.0, v11
	v_mul_f32_e32 v3, v3, v10
	v_fmamk_f32 v10, v40, 0x3a800000, v234
	v_fmamk_f32 v8, v36, 0x3a800000, v238
	v_rcp_f32_e32 v11, v11
	v_med3_f32 v10, v10, s59, v189
	v_med3_f32 v8, v8, s59, v189
	v_add_f32_e32 v10, 1.0, v10
	v_add_f32_e32 v8, 1.0, v8
	v_fmamk_f32 v13, v49, 0x3a800000, v227
	v_fmamk_f32 v5, v45, 0x3a800000, v231
	v_mul_f32_e32 v7, v7, v10
	v_add_f32_e32 v10, 1.0, v12
	v_mul_f32_e32 v4, v4, v8
	v_min_f32_e32 v8, 0x40e00000, v13
	v_min_f32_e32 v5, 0x40e00000, v5
	v_rcp_f32_e32 v10, v10
	v_mul_f32_e32 v7, v7, v11
	v_mul_f32_e32 v11, 0x3fd9db23, v8
	v_mul_f32_e32 v12, 0x3fd9db23, v5
	v_mul_f32_e32 v11, 0xbfb8aa3b, v11
	v_mul_f32_e32 v12, 0xbfb8aa3b, v12
	v_exp_f32_e32 v11, v11
	v_exp_f32_e32 v12, v12
	v_fmamk_f32 v17, v41, 0x3a800000, v235
	v_mul_f32_e32 v4, v4, v10
	v_med3_f32 v10, v17, s59, v189
	v_fmamk_f32 v9, v37, 0x3a800000, v239
	v_med3_f32 v9, v9, s59, v189
	v_add_f32_e32 v10, 1.0, v10
	v_add_f32_e32 v11, 1.0, v11
	v_mul_f32_e32 v8, v8, v10
	v_add_f32_e32 v10, 1.0, v12
	v_add_f32_e32 v9, 1.0, v9
	v_rcp_f32_e32 v11, v11
	v_rcp_f32_e32 v10, v10
	v_mul_f32_e32 v5, v5, v9
	v_mul_f32_e32 v0, 4.0, v0
	v_mul_f32_e32 v9, 4.0, v2
	v_mov_b32_e32 v2, v171
	v_cvt_pk_fp8_f32 v2, v0, v9
	v_mul_f32_e32 v0, 4.0, v6
	v_mul_f32_e32 v6, 4.0, v3
	v_mov_b32_e32 v3, v171
	v_cvt_pk_fp8_f32 v3, v0, v6
	v_mul_f32_e32 v8, v8, v11
	v_mul_f32_e32 v5, v5, v10
	v_mul_f32_e32 v7, 4.0, v7
	v_mul_f32_e32 v8, 4.0, v8
	v_mul_f32_e32 v0, 4.0, v4
	v_mul_f32_e32 v4, 4.0, v5
	v_cvt_pk_fp8_f32 v2, v7, v8 op_sel:[0,0,1]
	v_cvt_pk_fp8_f32 v3, v0, v4 op_sel:[0,0,1]
	v_add_co_u32_e32 v4, vcc, 0x58000, v18
	s_nop 1
	v_addc_co_u32_e32 v5, vcc, 0, v19, vcc
	s_andn2_b64 vcc, exec, s[4:5]
	s_mov_b64 s[4:5], -1
	global_store_dwordx2 v[4:5], v[2:3], off nt
	s_cbranch_vccnz .LBB0_1470
	s_andn2_b64 vcc, exec, s[12:13]
	s_cbranch_vccnz .LBB0_1469
	s_barrier
	s_branch .LBB0_1469

.LBB0_1580:
	s_lshl_b32 s1, s38, 8
	s_ashr_i32 s0, s38, 3
	s_and_b32 s1, s1, 0x700
	v_or_b32_e32 v170, s1, v183
	v_mov_b32_e32 v16, v171
	v_mov_b32_e32 v17, v171
	v_mov_b32_e32 v18, v171
	v_mov_b32_e32 v19, v171
	v_mov_b32_e32 v20, v171
	v_mov_b32_e32 v21, v171
	v_lshl_add_u32 v10, s36, 8, v1
	v_ashrrev_i32_e32 v11, 31, v10
	v_or_b32_e32 v12, 16, v10
	v_or_b32_e32 v14, 32, v10
	v_or_b32_e32 v24, 48, v10
	v_lshlrev_b64 v[10:11], 11, v[10:11]
	v_ashrrev_i32_e32 v13, 31, v12
	v_ashrrev_i32_e32 v15, 31, v14
	v_lshl_add_u64 v[10:11], s[12:13], 0, v[10:11]
	v_lshlrev_b64 v[12:13], 11, v[12:13]
	v_lshlrev_b64 v[14:15], 11, v[14:15]
	v_lshl_add_u64 v[10:11], v[10:11], 0, v[170:171]
	v_lshl_add_u64 v[12:13], s[12:13], 0, v[12:13]
	v_lshl_add_u64 v[14:15], s[12:13], 0, v[14:15]
	v_mov_b32_e32 v22, v171
	v_lshl_add_u64 v[12:13], v[12:13], 0, v[170:171]
	v_lshl_add_u64 v[14:15], v[14:15], 0, v[170:171]
	v_pk_fma_f32 v[28:29], v[158:159], s[18:19], v[224:225] op_sel_hi:[1,0,1]
	v_pk_fma_f32 v[32:33], v[154:155], s[18:19], v[228:229] op_sel_hi:[1,0,1]
	v_pk_fma_f32 v[150:151], v[150:151], s[18:19], v[224:225] op_sel_hi:[1,0,1]
	v_pk_fma_f32 v[146:147], v[146:147], s[18:19], v[228:229] op_sel_hi:[1,0,1]
	v_mul_f32_e32 v23, 0x41800000, v28
	v_mul_f32_e32 v25, 0x41800000, v29
	v_mul_f32_e32 v28, 0x41800000, v32
	v_mul_f32_e32 v29, 0x41800000, v33
	v_pk_fma_f32 v[142:143], v[142:143], s[18:19], v[224:225] op_sel_hi:[1,0,1]
	v_pk_fma_f32 v[138:139], v[138:139], s[18:19], v[228:229] op_sel_hi:[1,0,1]
	v_mul_f32_e32 v32, 0x41800000, v150
	v_mul_f32_e32 v33, 0x41800000, v151
	v_mul_f32_e32 v146, 0x41800000, v146
	v_mul_f32_e32 v147, 0x41800000, v147
	v_cvt_pk_fp8_f32 v16, v23, v25
	v_cvt_pk_fp8_f32 v17, v28, v29
	v_mul_f32_e32 v142, 0x41800000, v142
	v_mul_f32_e32 v143, 0x41800000, v143
	v_mul_f32_e32 v138, 0x41800000, v138
	v_mul_f32_e32 v139, 0x41800000, v139
	v_cvt_pk_fp8_f32 v18, v32, v33
	v_cvt_pk_fp8_f32 v19, v146, v147
	v_pk_fma_f32 v[26:27], v[160:161], s[18:19], v[226:227] op_sel_hi:[1,0,1]
	v_pk_fma_f32 v[30:31], v[156:157], s[18:19], v[230:231] op_sel_hi:[1,0,1]
	v_cvt_pk_fp8_f32 v20, v142, v143
	v_cvt_pk_fp8_f32 v21, v138, v139
	v_pk_fma_f32 v[152:153], v[152:153], s[18:19], v[226:227] op_sel_hi:[1,0,1]
	v_pk_fma_f32 v[148:149], v[148:149], s[18:19], v[230:231] op_sel_hi:[1,0,1]
	v_mul_f32_e32 v26, 0x41800000, v26
	v_mul_f32_e32 v27, 0x41800000, v27
	v_mul_f32_e32 v30, 0x41800000, v30
	v_mul_f32_e32 v31, 0x41800000, v31
	v_pk_fma_f32 v[144:145], v[144:145], s[18:19], v[226:227] op_sel_hi:[1,0,1]
	v_pk_fma_f32 v[140:141], v[140:141], s[18:19], v[230:231] op_sel_hi:[1,0,1]
	v_mul_f32_e32 v150, 0x41800000, v152
	v_mul_f32_e32 v151, 0x41800000, v153
	v_mul_f32_e32 v148, 0x41800000, v148
	v_mul_f32_e32 v149, 0x41800000, v149
	v_cvt_pk_fp8_f32 v16, v26, v27 op_sel:[0,0,1]
	v_cvt_pk_fp8_f32 v17, v30, v31 op_sel:[0,0,1]
	v_mul_f32_e32 v144, 0x41800000, v144
	v_mul_f32_e32 v145, 0x41800000, v145
	v_mul_f32_e32 v140, 0x41800000, v140
	v_mul_f32_e32 v141, 0x41800000, v141
	v_cvt_pk_fp8_f32 v18, v150, v151 op_sel:[0,0,1]
	v_cvt_pk_fp8_f32 v19, v148, v149 op_sel:[0,0,1]
	v_cvt_pk_fp8_f32 v20, v144, v145 op_sel:[0,0,1]
	v_cvt_pk_fp8_f32 v21, v140, v141 op_sel:[0,0,1]
	v_pk_fma_f32 v[134:135], v[134:135], s[18:19], v[224:225] op_sel_hi:[1,0,1]
	v_pk_fma_f32 v[130:131], v[130:131], s[18:19], v[228:229] op_sel_hi:[1,0,1]
	v_mul_f32_e32 v134, 0x41800000, v134
	v_mul_f32_e32 v135, 0x41800000, v135
	v_mul_f32_e32 v130, 0x41800000, v130
	global_store_dwordx2 v[10:11], v[16:17], off nt
	global_store_dwordx2 v[12:13], v[18:19], off nt
	global_store_dwordx2 v[14:15], v[20:21], off nt
	v_mul_f32_e32 v16, 0x41800000, v131
	v_mov_b32_e32 v23, v171
	v_cvt_pk_fp8_f32 v22, v134, v135
	v_cvt_pk_fp8_f32 v23, v130, v16
	v_pk_fma_f32 v[136:137], v[136:137], s[18:19], v[226:227] op_sel_hi:[1,0,1]
	v_pk_fma_f32 v[132:133], v[132:133], s[18:19], v[230:231] op_sel_hi:[1,0,1]
	v_mul_f32_e32 v136, 0x41800000, v136
	v_mul_f32_e32 v137, 0x41800000, v137
	v_mul_f32_e32 v16, 0x41800000, v132
	v_mul_f32_e32 v17, 0x41800000, v133
	v_ashrrev_i32_e32 v25, 31, v24
	v_pk_fma_f32 v[18:19], v[128:129], s[18:19], v[226:227] op_sel_hi:[1,0,1]
	v_pk_fma_f32 v[20:21], v[126:127], s[18:19], v[224:225] op_sel_hi:[1,0,1]
	v_cvt_pk_fp8_f32 v22, v136, v137 op_sel:[0,0,1]
	v_cvt_pk_fp8_f32 v23, v16, v17 op_sel:[0,0,1]
	v_lshlrev_b64 v[16:17], 11, v[24:25]
	v_pk_fma_f32 v[24:25], v[122:123], s[18:19], v[228:229] op_sel_hi:[1,0,1]
	v_mul_f32_e32 v20, 0x41800000, v20
	v_mul_f32_e32 v21, 0x41800000, v21
	v_mul_f32_e32 v26, 0x41800000, v18
	v_mov_b32_e32 v18, v171
	v_mul_f32_e32 v27, 0x41800000, v19
	v_cvt_pk_fp8_f32 v18, v20, v21
	v_mul_f32_e32 v20, 0x41800000, v24
	v_mul_f32_e32 v21, 0x41800000, v25
	v_mov_b32_e32 v19, v171
	v_lshl_add_u64 v[16:17], s[12:13], 0, v[16:17]
	v_cvt_pk_fp8_f32 v19, v20, v21
	v_lshl_add_u64 v[16:17], v[16:17], 0, v[170:171]
	global_store_dwordx2 v[16:17], v[22:23], off nt
	v_pk_fma_f32 v[22:23], v[124:125], s[18:19], v[230:231] op_sel_hi:[1,0,1]
	v_cvt_pk_fp8_f32 v18, v26, v27 op_sel:[0,0,1]
	v_mul_f32_e32 v20, 0x41800000, v22
	v_mul_f32_e32 v21, 0x41800000, v23
	v_cvt_pk_fp8_f32 v19, v20, v21 op_sel:[0,0,1]
	v_add_co_u32_e32 v20, vcc, s64, v10
	v_pk_fma_f32 v[24:25], v[114:115], s[18:19], v[228:229] op_sel_hi:[1,0,1]
	s_nop 0
	v_addc_co_u32_e32 v21, vcc, 0, v11, vcc
	global_store_dwordx2 v[20:21], v[18:19], off nt
	v_pk_fma_f32 v[18:19], v[120:121], s[18:19], v[226:227] op_sel_hi:[1,0,1]
	v_pk_fma_f32 v[20:21], v[118:119], s[18:19], v[224:225] op_sel_hi:[1,0,1]
	v_mul_f32_e32 v26, 0x41800000, v18
	v_mul_f32_e32 v20, 0x41800000, v20
	v_mul_f32_e32 v21, 0x41800000, v21
	v_mov_b32_e32 v18, v171
	v_mul_f32_e32 v27, 0x41800000, v19
	v_cvt_pk_fp8_f32 v18, v20, v21
	v_mul_f32_e32 v20, 0x41800000, v24
	v_mul_f32_e32 v21, 0x41800000, v25
	v_mov_b32_e32 v19, v171
	v_cvt_pk_fp8_f32 v19, v20, v21
	v_pk_fma_f32 v[22:23], v[116:117], s[18:19], v[230:231] op_sel_hi:[1,0,1]
	v_cvt_pk_fp8_f32 v18, v26, v27 op_sel:[0,0,1]
	v_mul_f32_e32 v20, 0x41800000, v22
	v_mul_f32_e32 v21, 0x41800000, v23
	v_cvt_pk_fp8_f32 v19, v20, v21 op_sel:[0,0,1]
	v_add_co_u32_e32 v20, vcc, s65, v10
	v_pk_fma_f32 v[24:25], v[106:107], s[18:19], v[228:229] op_sel_hi:[1,0,1]
	s_nop 0
	v_addc_co_u32_e32 v21, vcc, 0, v11, vcc
	global_store_dwordx2 v[20:21], v[18:19], off nt
	v_pk_fma_f32 v[18:19], v[112:113], s[18:19], v[226:227] op_sel_hi:[1,0,1]
	v_pk_fma_f32 v[20:21], v[110:111], s[18:19], v[224:225] op_sel_hi:[1,0,1]
	v_mul_f32_e32 v26, 0x41800000, v18
	v_mul_f32_e32 v20, 0x41800000, v20
	v_mul_f32_e32 v21, 0x41800000, v21
	v_mov_b32_e32 v18, v171
	v_mul_f32_e32 v27, 0x41800000, v19
	v_cvt_pk_fp8_f32 v18, v20, v21
	v_mul_f32_e32 v20, 0x41800000, v24
	v_mul_f32_e32 v21, 0x41800000, v25
	v_mov_b32_e32 v19, v171
	v_cvt_pk_fp8_f32 v19, v20, v21
	v_pk_fma_f32 v[22:23], v[108:109], s[18:19], v[230:231] op_sel_hi:[1,0,1]
	v_cvt_pk_fp8_f32 v18, v26, v27 op_sel:[0,0,1]
	v_mul_f32_e32 v20, 0x41800000, v22
	v_mul_f32_e32 v21, 0x41800000, v23
	v_cvt_pk_fp8_f32 v19, v20, v21 op_sel:[0,0,1]
	v_add_co_u32_e32 v20, vcc, s66, v10
	v_pk_fma_f32 v[6:7], v[94:95], s[18:19], v[224:225] op_sel_hi:[1,0,1]
	s_nop 0
	v_addc_co_u32_e32 v21, vcc, 0, v11, vcc
	global_store_dwordx2 v[20:21], v[18:19], off nt
	v_pk_fma_f32 v[2:3], v[90:91], s[18:19], v[228:229] op_sel_hi:[1,0,1]
	v_mul_f32_e32 v18, 0x41800000, v6
	v_mul_f32_e32 v7, 0x41800000, v7
	v_mov_b32_e32 v6, v171
	v_cvt_pk_fp8_f32 v6, v18, v7
	v_mul_f32_e32 v2, 0x41800000, v2
	v_mul_f32_e32 v3, 0x41800000, v3
	v_mov_b32_e32 v7, v171
	v_cvt_pk_fp8_f32 v7, v2, v3
	v_pk_fma_f32 v[8:9], v[96:97], s[18:19], v[226:227] op_sel_hi:[1,0,1]
	v_pk_fma_f32 v[4:5], v[92:93], s[18:19], v[230:231] op_sel_hi:[1,0,1]
	v_mul_f32_e32 v8, 0x41800000, v8
	v_mul_f32_e32 v9, 0x41800000, v9
	v_mul_f32_e32 v2, 0x41800000, v4
	v_mul_f32_e32 v3, 0x41800000, v5
	v_cvt_pk_fp8_f32 v6, v8, v9 op_sel:[0,0,1]
	v_cvt_pk_fp8_f32 v7, v2, v3 op_sel:[0,0,1]
	v_add_co_u32_e32 v2, vcc, s67, v10
	v_lshl_add_u64 v[18:19], v[10:11], 0, s[8:9]
	s_nop 0
	v_addc_co_u32_e32 v3, vcc, 0, v11, vcc
	global_store_dwordx2 v[2:3], v[6:7], off nt
	s_nop 0
	v_lshl_add_u64 v[20:21], v[10:11], 0, s[20:21]
	v_lshl_add_u64 v[22:23], v[10:11], 0, s[22:23]
	v_lshl_add_u64 v[24:25], v[10:11], 0, s[24:25]
	s_andn2_b64 vcc, exec, s[4:5]
	s_mov_b64 s[4:5], -1
	v_pk_fma_f32 v[26:27], v[104:105], s[18:19], v[234:235] op_sel_hi:[1,0,1]
	v_pk_fma_f32 v[28:29], v[102:103], s[18:19], v[232:233] op_sel_hi:[1,0,1]
	v_pk_fma_f32 v[32:33], v[98:99], s[18:19], v[236:237] op_sel_hi:[1,0,1]
	v_mul_f32_e32 v0, 0x41800000, v28
	v_mul_f32_e32 v28, 0x41800000, v29
	v_mul_f32_e32 v29, 0x41800000, v26
	v_mov_b32_e32 v26, v171
	v_mul_f32_e32 v90, 0x41800000, v27
	v_cvt_pk_fp8_f32 v26, v0, v28
	v_mul_f32_e32 v0, 0x41800000, v32
	v_mul_f32_e32 v28, 0x41800000, v33
	v_mov_b32_e32 v27, v171
	v_cvt_pk_fp8_f32 v27, v0, v28
	v_pk_fma_f32 v[30:31], v[100:101], s[18:19], v[238:239] op_sel_hi:[1,0,1]
	v_cvt_pk_fp8_f32 v26, v29, v90 op_sel:[0,0,1]
	v_mul_f32_e32 v0, 0x41800000, v30
	v_mul_f32_e32 v28, 0x41800000, v31
	v_cvt_pk_fp8_f32 v27, v0, v28 op_sel:[0,0,1]
	v_pk_fma_f32 v[28:29], v[88:89], s[18:19], v[234:235] op_sel_hi:[1,0,1]
	v_pk_fma_f32 v[30:31], v[86:87], s[18:19], v[232:233] op_sel_hi:[1,0,1]
	v_pk_fma_f32 v[82:83], v[82:83], s[18:19], v[236:237] op_sel_hi:[1,0,1]
	v_mul_f32_e32 v0, 0x41800000, v30
	v_mul_f32_e32 v30, 0x41800000, v31
	v_mul_f32_e32 v31, 0x41800000, v28
	v_mov_b32_e32 v28, v171
	v_pk_fma_f32 v[32:33], v[84:85], s[18:19], v[238:239] op_sel_hi:[1,0,1]
	v_mul_f32_e32 v84, 0x41800000, v29
	v_cvt_pk_fp8_f32 v28, v0, v30
	v_mul_f32_e32 v0, 0x41800000, v82
	v_mul_f32_e32 v30, 0x41800000, v83
	v_mov_b32_e32 v29, v171
	v_cvt_pk_fp8_f32 v29, v0, v30
	v_mul_f32_e32 v0, 0x41800000, v32
	v_mul_f32_e32 v30, 0x41800000, v33
	v_cvt_pk_fp8_f32 v28, v31, v84 op_sel:[0,0,1]
	v_cvt_pk_fp8_f32 v29, v0, v30 op_sel:[0,0,1]
	v_pk_fma_f32 v[30:31], v[80:81], s[18:19], v[234:235] op_sel_hi:[1,0,1]
	v_pk_fma_f32 v[32:33], v[78:79], s[18:19], v[232:233] op_sel_hi:[1,0,1]
	v_pk_fma_f32 v[74:75], v[74:75], s[18:19], v[236:237] op_sel_hi:[1,0,1]
	v_mul_f32_e32 v0, 0x41800000, v32
	v_mul_f32_e32 v32, 0x41800000, v33
	v_mul_f32_e32 v33, 0x41800000, v30
	v_mov_b32_e32 v30, v171
	v_mul_f32_e32 v78, 0x41800000, v31
	v_cvt_pk_fp8_f32 v30, v0, v32
	v_mul_f32_e32 v0, 0x41800000, v74
	v_mul_f32_e32 v32, 0x41800000, v75
	v_mov_b32_e32 v31, v171
	v_cvt_pk_fp8_f32 v31, v0, v32
	v_pk_fma_f32 v[76:77], v[76:77], s[18:19], v[238:239] op_sel_hi:[1,0,1]
	v_cvt_pk_fp8_f32 v30, v33, v78 op_sel:[0,0,1]
	v_mul_f32_e32 v0, 0x41800000, v76
	v_mul_f32_e32 v32, 0x41800000, v77
	v_cvt_pk_fp8_f32 v31, v0, v32 op_sel:[0,0,1]
	v_pk_fma_f32 v[32:33], v[72:73], s[18:19], v[234:235] op_sel_hi:[1,0,1]
	v_pk_fma_f32 v[70:71], v[70:71], s[18:19], v[232:233] op_sel_hi:[1,0,1]
	v_pk_fma_f32 v[66:67], v[66:67], s[18:19], v[236:237] op_sel_hi:[1,0,1]
	v_mul_f32_e32 v0, 0x41800000, v70
	v_mul_f32_e32 v70, 0x41800000, v71
	v_mul_f32_e32 v71, 0x41800000, v32
	v_mov_b32_e32 v32, v171
	v_mul_f32_e32 v72, 0x41800000, v33
	v_cvt_pk_fp8_f32 v32, v0, v70
	v_mul_f32_e32 v0, 0x41800000, v66
	v_mul_f32_e32 v66, 0x41800000, v67
	v_mov_b32_e32 v33, v171
	v_cvt_pk_fp8_f32 v33, v0, v66
	v_pk_fma_f32 v[68:69], v[68:69], s[18:19], v[238:239] op_sel_hi:[1,0,1]
	v_cvt_pk_fp8_f32 v32, v71, v72 op_sel:[0,0,1]
	v_mul_f32_e32 v0, 0x41800000, v68
	v_mul_f32_e32 v66, 0x41800000, v69
	v_cvt_pk_fp8_f32 v33, v0, v66 op_sel:[0,0,1]
	global_store_dwordx2 v[10:11], v[26:27], off offset:128 nt
	global_store_dwordx2 v[12:13], v[28:29], off offset:128 nt
	global_store_dwordx2 v[14:15], v[30:31], off offset:128 nt
	global_store_dwordx2 v[16:17], v[32:33], off offset:128 nt
	v_pk_fma_f32 v[10:11], v[64:65], s[18:19], v[234:235] op_sel_hi:[1,0,1]
	v_pk_fma_f32 v[12:13], v[62:63], s[18:19], v[232:233] op_sel_hi:[1,0,1]
	v_pk_fma_f32 v[16:17], v[58:59], s[18:19], v[236:237] op_sel_hi:[1,0,1]
	v_mul_f32_e32 v0, 0x41800000, v12
	v_mul_f32_e32 v12, 0x41800000, v13
	v_mul_f32_e32 v13, 0x41800000, v10
	v_mov_b32_e32 v10, v171
	v_mul_f32_e32 v26, 0x41800000, v11
	v_cvt_pk_fp8_f32 v10, v0, v12
	v_mul_f32_e32 v0, 0x41800000, v16
	v_mul_f32_e32 v12, 0x41800000, v17
	v_mov_b32_e32 v11, v171
	v_cvt_pk_fp8_f32 v11, v0, v12
	v_pk_fma_f32 v[14:15], v[60:61], s[18:19], v[238:239] op_sel_hi:[1,0,1]
	v_cvt_pk_fp8_f32 v10, v13, v26 op_sel:[0,0,1]
	v_mul_f32_e32 v0, 0x41800000, v14
	v_mul_f32_e32 v12, 0x41800000, v15
	v_cvt_pk_fp8_f32 v11, v0, v12 op_sel:[0,0,1]
	v_pk_fma_f32 v[12:13], v[56:57], s[18:19], v[234:235] op_sel_hi:[1,0,1]
	v_pk_fma_f32 v[14:15], v[54:55], s[18:19], v[232:233] op_sel_hi:[1,0,1]
	v_pk_fma_f32 v[26:27], v[50:51], s[18:19], v[236:237] op_sel_hi:[1,0,1]
	v_mul_f32_e32 v0, 0x41800000, v14
	v_mul_f32_e32 v14, 0x41800000, v15
	v_mul_f32_e32 v15, 0x41800000, v12
	v_mov_b32_e32 v12, v171
	v_mul_f32_e32 v28, 0x41800000, v13
	v_cvt_pk_fp8_f32 v12, v0, v14
	v_mul_f32_e32 v0, 0x41800000, v26
	v_mul_f32_e32 v14, 0x41800000, v27
	v_mov_b32_e32 v13, v171
	v_cvt_pk_fp8_f32 v13, v0, v14
	v_pk_fma_f32 v[16:17], v[52:53], s[18:19], v[238:239] op_sel_hi:[1,0,1]
	v_cvt_pk_fp8_f32 v12, v15, v28 op_sel:[0,0,1]
	v_mul_f32_e32 v0, 0x41800000, v16
	v_mul_f32_e32 v14, 0x41800000, v17
	v_cvt_pk_fp8_f32 v13, v0, v14 op_sel:[0,0,1]
	v_pk_fma_f32 v[14:15], v[48:49], s[18:19], v[234:235] op_sel_hi:[1,0,1]
	v_pk_fma_f32 v[16:17], v[46:47], s[18:19], v[232:233] op_sel_hi:[1,0,1]
	v_pk_fma_f32 v[28:29], v[42:43], s[18:19], v[236:237] op_sel_hi:[1,0,1]
	v_mul_f32_e32 v0, 0x41800000, v16
	v_mul_f32_e32 v16, 0x41800000, v17
	v_mul_f32_e32 v17, 0x41800000, v14
	v_mov_b32_e32 v14, v171
	v_mul_f32_e32 v30, 0x41800000, v15
	v_cvt_pk_fp8_f32 v14, v0, v16
	v_mul_f32_e32 v0, 0x41800000, v28
	v_mul_f32_e32 v16, 0x41800000, v29
	v_mov_b32_e32 v15, v171
	v_cvt_pk_fp8_f32 v15, v0, v16
	v_pk_fma_f32 v[26:27], v[44:45], s[18:19], v[238:239] op_sel_hi:[1,0,1]
	v_pk_fma_f32 v[2:3], v[38:39], s[18:19], v[232:233] op_sel_hi:[1,0,1]
	v_mul_f32_e32 v0, 0x41800000, v26
	v_mul_f32_e32 v16, 0x41800000, v27
	v_cvt_pk_fp8_f32 v15, v0, v16 op_sel:[0,0,1]
	v_pk_fma_f32 v[6:7], v[34:35], s[18:19], v[236:237] op_sel_hi:[1,0,1]
	v_mul_f32_e32 v0, 0x41800000, v2
	v_mul_f32_e32 v3, 0x41800000, v3
	v_mov_b32_e32 v2, v171
	v_cvt_pk_fp8_f32 v2, v0, v3
	v_mul_f32_e32 v0, 0x41800000, v6
	v_mul_f32_e32 v6, 0x41800000, v7
	v_mov_b32_e32 v3, v171
	v_cvt_pk_fp8_f32 v3, v0, v6
	v_pk_fma_f32 v[4:5], v[40:41], s[18:19], v[234:235] op_sel_hi:[1,0,1]
	v_pk_fma_f32 v[8:9], v[36:37], s[18:19], v[238:239] op_sel_hi:[1,0,1]
	v_mul_f32_e32 v4, 0x41800000, v4
	v_mul_f32_e32 v5, 0x41800000, v5
	v_cvt_pk_fp8_f32 v14, v17, v30 op_sel:[0,0,1]
	v_cvt_pk_fp8_f32 v2, v4, v5 op_sel:[0,0,1]
	v_mul_f32_e32 v0, 0x41800000, v8
	v_mul_f32_e32 v4, 0x41800000, v9
	v_cvt_pk_fp8_f32 v3, v0, v4 op_sel:[0,0,1]
	global_store_dwordx2 v[18:19], v[10:11], off offset:128 nt
	global_store_dwordx2 v[20:21], v[12:13], off offset:128 nt
	global_store_dwordx2 v[22:23], v[14:15], off offset:128 nt
	global_store_dwordx2 v[24:25], v[2:3], off offset:128 nt
	s_cbranch_vccnz .LBB0_1565
	s_andn2_b64 vcc, exec, s[10:11]
	s_cbranch_vccnz .LBB0_1564
	s_barrier
	s_branch .LBB0_1564
